# baseline (speedup 1.0000x reference)
_Z22k2_resolve_rank_gatherPKfS0_PKdS0_PKiPKyPKtS0_S4_Pf:
	s_load_dwordx16 s[4:19], s[0:1], 0x0
	s_load_dwordx4 s[20:23], s[0:1], 0x40
	s_and_b32 s3, s2, 7
	s_lshr_b32 s2, s2, 3
	s_lshl_b32 s3, s3, 7
	s_add_u32 s2, s2, s3
	v_and_b32_e32 v1, 0x3ff, v0
	s_lshr_b32 s24, s2, 6
	s_and_b32 s25, s2, 63
	s_lshl_b32 s26, s24, 9
	v_lshl_add_u32 v2, v1, 1, s26
	v_lshlrev_b32_e32 v3, 4, v2
	v_lshlrev_b32_e32 v24, 2, v2
	v_lshlrev_b32_e32 v25, 3, v2
	v_mov_b32_e32 v106, 0
	v_mov_b32_e32 v107, 0
	v_mov_b32_e32 v105, 0x1800
	v_lshlrev_b32_e32 v104, 3, v1
	s_movk_i32 s30, 0x641
	s_mov_b32 s32, 0xa0b5ed8d
	s_mov_b32 s33, 0x3ed0c6f7
	s_mov_b32 s34, 0xa0b5ed8d
	s_mov_b32 s35, 0xbed0c6f7
	s_mul_i32 s31, s26, 0x1904
	v_lshrrev_b32_e32 v29, 6, v1
	s_waitcnt lgkmcnt(0)
	global_load_dwordx4 v[4:7], v3, s[16:17]
	global_load_dwordx4 v[8:11], v3, s[16:17] offset:16
	global_load_dwordx2 v[12:13], v24, s[10:11]
	global_load_dwordx2 v[16:17], v24, s[12:13]
	global_load_dwordx4 v[20:23], v25, s[8:9]
	global_load_dwordx2 v[14:15], v24, s[18:19]
	global_load_dwordx2 v[18:19], v24, s[20:21]
	s_add_u32 s28, s4, s31
	s_addc_u32 s29, s5, 0
	v_readfirstlane_b32 s27, v29
	ds_write_b64 v105, v[106:107]
	ds_write_b64 v105, v[106:107] offset:8
	ds_write_b64 v105, v[106:107] offset:16
	ds_write_b64 v105, v[106:107] offset:24
	ds_write_b64 v104, v[106:107] offset:8448
	s_mov_b64 s[36:37], 0
	s_mov_b64 s[38:39], 0
	s_mov_b64 s[40:41], 0
	s_mov_b64 s[42:43], 0
	s_mov_b64 s[44:45], 0
	v_lshlrev_b32_e32 v2, 4, v1
	s_waitcnt vmcnt(2)
	ds_write_b128 v2, v[20:23] offset:12544
	v_lshlrev_b32_e32 v3, 5, v1
	ds_write_b128 v3, v[4:7] offset:22784
	ds_write_b128 v3, v[8:11] offset:22800
	ds_write_b64 v104, v[16:17] offset:30976
	v_and_b32_e32 v26, 0xffff, v4
	v_and_b32_e32 v27, 0xffff, v8
	v_max_u32_e32 v28, v26, v27
	v_cvt_f64_f32_e32 v[92:93], v12
	v_cvt_f64_f32_e32 v[94:95], v13
	v_add_f64 v[92:93], v[92:93], -v[20:21]
	v_add_f64 v[94:95], v[94:95], -v[22:23]
	ds_write_b128 v2, v[92:95] offset:0
	ds_write_b64 v104, v[12:13] offset:4096
	s_waitcnt vmcnt(0)
	ds_write_b64 v104, v[14:15] offset:33024
	v_cvt_f64_f32_e32 v[96:97], v14
	v_cvt_f64_f32_e32 v[98:99], v15
	v_add_f64 v[96:97], v[96:97], -v[20:21]
	v_add_f64 v[98:99], v[98:99], -v[22:23]
	s_waitcnt lgkmcnt(0)
	s_barrier
	v_cmp_lt_u32_e32 vcc, 0, v28
	s_cbranch_vccz .Lk2_l1_done
	v_cmp_lt_u32_e32 vcc, 0, v26
	s_and_saveexec_b64 s[46:47], vcc
	s_cbranch_execz .Lk2_l1_0_0
	v_lshrrev_b32_e32 v29, 16, v4
	v_mad_u32_u24 v30, v29, s30, v16
	v_lshlrev_b32_e32 v30, 2, v30
	v_lshlrev_b32_e32 v29, 3, v29
	global_load_dword v32, v30, s[28:29] nt
	ds_read_b64 v[34:35], v29 offset:12544
.Lk2_l1_0_0:
	s_or_b64 exec, exec, s[46:47]
	v_cmp_lt_u32_e32 vcc, 0, v27
	s_and_saveexec_b64 s[46:47], vcc
	s_cbranch_execz .Lk2_l1_0_1
	v_lshrrev_b32_e32 v29, 16, v8
	v_mad_u32_u24 v30, v29, s30, v17
	v_lshlrev_b32_e32 v30, 2, v30
	v_lshlrev_b32_e32 v29, 3, v29
	global_load_dword v36, v30, s[28:29] nt
	ds_read_b64 v[38:39], v29 offset:12544
.Lk2_l1_0_1:
	s_or_b64 exec, exec, s[46:47]
	v_cmp_lt_u32_e32 vcc, 1, v28
	s_cbranch_vccz .Lk2_l1_done
	v_cmp_lt_u32_e32 vcc, 1, v26
	s_and_saveexec_b64 s[46:47], vcc
	s_cbranch_execz .Lk2_l1_1_0
	v_and_b32_e32 v29, 0xffff, v5
	v_mad_u32_u24 v30, v29, s30, v16
	v_lshlrev_b32_e32 v30, 2, v30
	v_lshlrev_b32_e32 v29, 3, v29
	global_load_dword v40, v30, s[28:29] nt
	ds_read_b64 v[42:43], v29 offset:12544
.Lk2_l1_1_0:
	s_or_b64 exec, exec, s[46:47]
	v_cmp_lt_u32_e32 vcc, 1, v27
	s_and_saveexec_b64 s[46:47], vcc
	s_cbranch_execz .Lk2_l1_1_1
	v_and_b32_e32 v29, 0xffff, v9
	v_mad_u32_u24 v30, v29, s30, v17
	v_lshlrev_b32_e32 v30, 2, v30
	v_lshlrev_b32_e32 v29, 3, v29
	global_load_dword v44, v30, s[28:29] nt
	ds_read_b64 v[46:47], v29 offset:12544
.Lk2_l1_1_1:
	s_or_b64 exec, exec, s[46:47]
	v_cmp_lt_u32_e32 vcc, 2, v28
	s_cbranch_vccz .Lk2_l1_done
	v_cmp_lt_u32_e32 vcc, 2, v26
	s_and_saveexec_b64 s[46:47], vcc
	s_cbranch_execz .Lk2_l1_2_0
	v_lshrrev_b32_e32 v29, 16, v5
	v_mad_u32_u24 v30, v29, s30, v16
	v_lshlrev_b32_e32 v30, 2, v30
	v_lshlrev_b32_e32 v29, 3, v29
	global_load_dword v48, v30, s[28:29] nt
	ds_read_b64 v[50:51], v29 offset:12544
.Lk2_l1_2_0:
	s_or_b64 exec, exec, s[46:47]
	v_cmp_lt_u32_e32 vcc, 2, v27
	s_and_saveexec_b64 s[46:47], vcc
	s_cbranch_execz .Lk2_l1_2_1
	v_lshrrev_b32_e32 v29, 16, v9
	v_mad_u32_u24 v30, v29, s30, v17
	v_lshlrev_b32_e32 v30, 2, v30
	v_lshlrev_b32_e32 v29, 3, v29
	global_load_dword v52, v30, s[28:29] nt
	ds_read_b64 v[54:55], v29 offset:12544
.Lk2_l1_2_1:
	s_or_b64 exec, exec, s[46:47]
	v_cmp_lt_u32_e32 vcc, 3, v28
	s_cbranch_vccz .Lk2_l1_done
	v_cmp_lt_u32_e32 vcc, 3, v26
	s_and_saveexec_b64 s[46:47], vcc
	s_cbranch_execz .Lk2_l1_3_0
	v_and_b32_e32 v29, 0xffff, v6
	v_mad_u32_u24 v30, v29, s30, v16
	v_lshlrev_b32_e32 v30, 2, v30
	v_lshlrev_b32_e32 v29, 3, v29
	global_load_dword v56, v30, s[28:29] nt
	ds_read_b64 v[58:59], v29 offset:12544
.Lk2_l1_3_0:
	s_or_b64 exec, exec, s[46:47]
	v_cmp_lt_u32_e32 vcc, 3, v27
	s_and_saveexec_b64 s[46:47], vcc
	s_cbranch_execz .Lk2_l1_3_1
	v_and_b32_e32 v29, 0xffff, v10
	v_mad_u32_u24 v30, v29, s30, v17
	v_lshlrev_b32_e32 v30, 2, v30
	v_lshlrev_b32_e32 v29, 3, v29
	global_load_dword v60, v30, s[28:29] nt
	ds_read_b64 v[62:63], v29 offset:12544
.Lk2_l1_3_1:
	s_or_b64 exec, exec, s[46:47]
	v_cmp_lt_u32_e32 vcc, 4, v28
	s_cbranch_vccz .Lk2_l1_done
	v_cmp_lt_u32_e32 vcc, 4, v26
	s_and_saveexec_b64 s[46:47], vcc
	s_cbranch_execz .Lk2_l1_4_0
	v_lshrrev_b32_e32 v29, 16, v6
	v_mad_u32_u24 v30, v29, s30, v16
	v_lshlrev_b32_e32 v30, 2, v30
	v_lshlrev_b32_e32 v29, 3, v29
	global_load_dword v64, v30, s[28:29] nt
	ds_read_b64 v[66:67], v29 offset:12544
.Lk2_l1_4_0:
	s_or_b64 exec, exec, s[46:47]
	v_cmp_lt_u32_e32 vcc, 4, v27
	s_and_saveexec_b64 s[46:47], vcc
	s_cbranch_execz .Lk2_l1_4_1
	v_lshrrev_b32_e32 v29, 16, v10
	v_mad_u32_u24 v30, v29, s30, v17
	v_lshlrev_b32_e32 v30, 2, v30
	v_lshlrev_b32_e32 v29, 3, v29
	global_load_dword v68, v30, s[28:29] nt
	ds_read_b64 v[70:71], v29 offset:12544
.Lk2_l1_4_1:
	s_or_b64 exec, exec, s[46:47]
	v_cmp_lt_u32_e32 vcc, 5, v28
	s_cbranch_vccz .Lk2_l1_done
	v_cmp_lt_u32_e32 vcc, 5, v26
	s_and_saveexec_b64 s[46:47], vcc
	s_cbranch_execz .Lk2_l1_5_0
	v_and_b32_e32 v29, 0xffff, v7
	v_mad_u32_u24 v30, v29, s30, v16
	v_lshlrev_b32_e32 v30, 2, v30
	v_lshlrev_b32_e32 v29, 3, v29
	global_load_dword v72, v30, s[28:29] nt
	ds_read_b64 v[74:75], v29 offset:12544
.Lk2_l1_5_0:
	s_or_b64 exec, exec, s[46:47]
	v_cmp_lt_u32_e32 vcc, 5, v27
	s_and_saveexec_b64 s[46:47], vcc
	s_cbranch_execz .Lk2_l1_5_1
	v_and_b32_e32 v29, 0xffff, v11
	v_mad_u32_u24 v30, v29, s30, v17
	v_lshlrev_b32_e32 v30, 2, v30
	v_lshlrev_b32_e32 v29, 3, v29
	global_load_dword v76, v30, s[28:29] nt
	ds_read_b64 v[78:79], v29 offset:12544
.Lk2_l1_5_1:
	s_or_b64 exec, exec, s[46:47]
	v_cmp_lt_u32_e32 vcc, 6, v28
	s_cbranch_vccz .Lk2_l1_done
	v_cmp_lt_u32_e32 vcc, 6, v26
	s_and_saveexec_b64 s[46:47], vcc
	s_cbranch_execz .Lk2_l1_6_0
	v_lshrrev_b32_e32 v29, 16, v7
	v_mad_u32_u24 v30, v29, s30, v16
	v_lshlrev_b32_e32 v30, 2, v30
	v_lshlrev_b32_e32 v29, 3, v29
	global_load_dword v80, v30, s[28:29] nt
	ds_read_b64 v[82:83], v29 offset:12544
.Lk2_l1_6_0:
	s_or_b64 exec, exec, s[46:47]
	v_cmp_lt_u32_e32 vcc, 6, v27
	s_and_saveexec_b64 s[46:47], vcc
	s_cbranch_execz .Lk2_l1_6_1
	v_lshrrev_b32_e32 v29, 16, v11
	v_mad_u32_u24 v30, v29, s30, v17
	v_lshlrev_b32_e32 v30, 2, v30
	v_lshlrev_b32_e32 v29, 3, v29
	global_load_dword v84, v30, s[28:29] nt
	ds_read_b64 v[86:87], v29 offset:12544
